# P1: RoPE cos/sin slab of each unit brought into unused LDS by LDS-DMA during the K loop, epilogue reads it with ds_read (no global loads behind the stores); plus m0 save/restore removal
# speedup vs baseline: 1.0081x; 1.0027x over previous
.LBB0_116:
	s_add_u32 s18, s4, 0x15c00000
	s_addc_u32 s19, s5, 0
	s_add_u32 s20, s4, 0x1200000
	s_addc_u32 s21, s5, 0
	s_lshl_b32 s4, s22, 5
	v_and_b32_e32 v4, 15, v2
	s_and_b32 s4, s4, 0x60
	v_lshlrev_b32_e32 v5, 7, v4
	v_or_b32_e32 v4, s4, v4
	s_add_u32 s4, s10, 0x80
	v_lshl_or_b32 v5, s6, 13, v5
	s_waitcnt vmcnt(2)
	s_barrier
	s_addc_u32 s5, s11, 0
	s_add_i32 s64, s56, 0x18000
	s_mov_b32 m0, s64
	s_nop 0
	global_load_lds_dwordx4 v215, s[4:5] offset:0
	s_add_i32 s65, s56, 0x1a000
	s_mov_b32 m0, s65
	s_nop 0
	global_load_lds_dwordx4 v216, s[4:5] offset:0
	s_add_u32 s22, s14, 0x80
	s_addc_u32 s23, s15, 0
	s_add_i32 s66, s56, 0x8000
	s_mov_b32 m0, s66
	s_nop 0
	global_load_lds_dwordx4 v211, s[22:23] offset:0
	s_add_i32 s67, s56, 0xa000
	s_mov_b32 m0, s67
	s_nop 0
	global_load_lds_dwordx4 v213, s[22:23] offset:0
	s_add_u32 s4, s10, 0x40080
	s_addc_u32 s5, s11, 0
	s_add_i32 s68, s56, 0x1c000
	s_add_i32 s69, s56, 0x1e000
	s_add_i32 s70, s56, 0xc000
	v_bfe_u32 v6, v2, 4, 2
	v_bfe_u32 v2, v2, 1, 3
	s_add_u32 s24, s14, 0x780
	v_bitop3_b32 v3, v3, v2, 3 bitop3:0x6c
	v_bitop3_b32 v2, v6, v2, 4 bitop3:0x36
	s_mov_b32 m0, s68
	s_nop 0
	global_load_lds_dwordx4 v215, s[4:5] offset:0
	s_addc_u32 s25, s15, 0
	v_lshlrev_b32_e32 v3, 4, v3
	v_lshlrev_b32_e32 v2, 4, v2
	v_lshlrev_b32_e32 v4, 7, v4
	s_mov_b32 m0, s69
	s_nop 0
	global_load_lds_dwordx4 v216, s[4:5] offset:0
	s_cmpk_lt_u32 s26, 0x100
	v_or_b32_e32 v217, v4, v3
	v_or_b32_e32 v218, v4, v2
	s_waitcnt vmcnt(6)
	s_cselect_b64 s[26:27], -1, 0
	s_add_i32 s4, 0, 0x10000
	v_or_b32_e32 v7, v3, v5
	v_or_b32_e32 v5, v2, v5
	v_add_u32_e32 v219, s4, v217
	v_add_u32_e32 v220, s4, v218
	s_add_i32 s4, 0, 0x14000
	s_add_i32 s71, s56, 0xe000
	s_ashr_i32 s72, s88, 31
	s_ashr_i32 s73, s82, 31
	v_add_u32_e32 v221, s4, v217
	v_add_u32_e32 v222, s4, v218
	v_add_u32_e32 v223, 0, v7
	v_add_u32_e32 v224, 0, v5
	s_mov_b64 s[28:29], 0x2000
	s_mov_b64 s[30:31], 0x2400
	s_mov_b64 s[34:35], 0x2800
	s_mov_b64 s[36:37], 0x2c00
	s_mov_b64 s[38:39], 0x80000
	s_mov_b32 s74, 0x80000
	s_mov_b64 s[40:41], 0x90000
	s_mov_b32 s75, 0x90000
	s_mov_b64 s[42:43], 0xa0000
	s_mov_b32 s76, 0xa0000
	s_mov_b64 s[44:45], 0xb0000
	v_mbcnt_hi_u32_b32 v225, -1, v1
	s_barrier
	v_readfirstlane_b32 s98, v0
	s_nop 3
	s_lshr_b32 s98, s98, 6
	s_lshl_b32 s99, s98, 10
	s_add_u32 s96, s20, s99
	s_addc_u32 s97, s21, 0
	s_add_u32 s98, s99, 0x20000
	v_bfe_u32 v255, v0, 8, 1
	v_lshlrev_b32_e32 v255, 6, v255
	v_and_or_b32 v255, v0, 15, v255
	v_lshlrev_b32_e32 v255, 6, v255
	v_add_u32_e32 v255, 0x20000, v255
	s_branch .LBB0_119

.LBB0_126:
	.p2align 3
	s_nop 0
	ds_read_b128 v[130:133], v219
	ds_read_b128 v[134:137], v219 offset:2048
	ds_read_b128 v[138:141], v220
	ds_read_b128 v[142:145], v220 offset:2048
	ds_read_b128 v[146:149], v221
	ds_read_b128 v[150:153], v221 offset:2048
	ds_read_b128 v[154:157], v222
	ds_read_b128 v[158:161], v222 offset:2048
	ds_read_b128 v[162:165], v223
	ds_read_b128 v[166:169], v223 offset:2048
	ds_read_b128 v[170:173], v224
	ds_read_b128 v[174:177], v224 offset:2048
	ds_read_b128 v[178:181], v223 offset:4096
	ds_read_b128 v[182:185], v223 offset:6144
	ds_read_b128 v[186:189], v224 offset:4096
	ds_read_b128 v[190:193], v224 offset:6144
	s_add_u32 s47, s14, s4
	s_addc_u32 s50, s15, s5
	s_add_u32 s54, s47, 0x80
	s_addc_u32 s55, s50, 0
	s_mov_b32 m0, s70
	s_nop 0
	global_load_lds_dwordx4 v212, s[54:55] offset:0
	s_nop 0
	s_mov_b32 m0, s71
	s_nop 0
	global_load_lds_dwordx4 v214, s[54:55] offset:0
	s_waitcnt vmcnt(8)
	s_waitcnt lgkmcnt(0)
	s_barrier
	s_setprio 1
	s_waitcnt lgkmcnt(7)
	v_mfma_f32_16x16x32_bf16 v[126:129], v[130:133], v[162:165], v[126:129]
	v_mfma_f32_16x16x32_bf16 v[122:125], v[134:137], v[162:165], v[122:125]
	s_waitcnt lgkmcnt(6)
	v_mfma_f32_16x16x32_bf16 v[118:121], v[130:133], v[166:169], v[118:121]
	v_mfma_f32_16x16x32_bf16 v[114:117], v[134:137], v[166:169], v[114:117]
	s_waitcnt lgkmcnt(3)
	v_mfma_f32_16x16x32_bf16 v[110:113], v[130:133], v[178:181], v[110:113]
	v_mfma_f32_16x16x32_bf16 v[106:109], v[134:137], v[178:181], v[106:109]
	s_waitcnt lgkmcnt(2)
	v_mfma_f32_16x16x32_bf16 v[102:105], v[130:133], v[182:185], v[102:105]
	v_mfma_f32_16x16x32_bf16 v[98:101], v[134:137], v[182:185], v[98:101]
	v_mfma_f32_16x16x32_bf16 v[126:129], v[138:141], v[170:173], v[126:129]
	v_mfma_f32_16x16x32_bf16 v[122:125], v[142:145], v[170:173], v[122:125]
	v_mfma_f32_16x16x32_bf16 v[118:121], v[138:141], v[174:177], v[118:121]
	v_mfma_f32_16x16x32_bf16 v[114:117], v[142:145], v[174:177], v[114:117]
	s_waitcnt lgkmcnt(1)
	v_mfma_f32_16x16x32_bf16 v[110:113], v[138:141], v[186:189], v[110:113]
	v_mfma_f32_16x16x32_bf16 v[106:109], v[142:145], v[186:189], v[106:109]
	s_waitcnt lgkmcnt(0)
	v_mfma_f32_16x16x32_bf16 v[102:105], v[138:141], v[190:193], v[102:105]
	v_mfma_f32_16x16x32_bf16 v[98:101], v[142:145], v[190:193], v[98:101]
	s_setprio 0
	s_setprio 1
	v_mfma_f32_16x16x32_bf16 v[94:97], v[146:149], v[162:165], v[94:97]
	v_mfma_f32_16x16x32_bf16 v[90:93], v[150:153], v[162:165], v[90:93]
	v_mfma_f32_16x16x32_bf16 v[86:89], v[146:149], v[166:169], v[86:89]
	v_mfma_f32_16x16x32_bf16 v[82:85], v[150:153], v[166:169], v[82:85]
	v_mfma_f32_16x16x32_bf16 v[78:81], v[146:149], v[178:181], v[78:81]
	v_mfma_f32_16x16x32_bf16 v[74:77], v[150:153], v[178:181], v[74:77]
	v_mfma_f32_16x16x32_bf16 v[70:73], v[146:149], v[182:185], v[70:73]
	v_mfma_f32_16x16x32_bf16 v[66:69], v[150:153], v[182:185], v[66:69]
	v_mfma_f32_16x16x32_bf16 v[94:97], v[154:157], v[170:173], v[94:97]
	v_mfma_f32_16x16x32_bf16 v[90:93], v[158:161], v[170:173], v[90:93]
	v_mfma_f32_16x16x32_bf16 v[86:89], v[154:157], v[174:177], v[86:89]
	v_mfma_f32_16x16x32_bf16 v[82:85], v[158:161], v[174:177], v[82:85]
	v_mfma_f32_16x16x32_bf16 v[78:81], v[154:157], v[186:189], v[78:81]
	v_mfma_f32_16x16x32_bf16 v[74:77], v[158:161], v[186:189], v[74:77]
	v_mfma_f32_16x16x32_bf16 v[70:73], v[154:157], v[190:193], v[70:73]
	v_mfma_f32_16x16x32_bf16 v[66:69], v[158:161], v[190:193], v[66:69]
	s_setprio 0
	s_barrier
	s_add_u32 s51, s10, s4
	s_addc_u32 s53, s11, s5
	ds_read_b128 v[162:165], v223 offset:16384
	ds_read_b128 v[166:169], v223 offset:18432
	ds_read_b128 v[170:173], v224 offset:16384
	ds_read_b128 v[174:177], v224 offset:18432
	ds_read_b128 v[178:181], v223 offset:20480
	ds_read_b128 v[182:185], v223 offset:22528
	ds_read_b128 v[186:189], v224 offset:20480
	ds_read_b128 v[190:193], v224 offset:22528
	s_add_u32 s54, s51, 0x100
	s_addc_u32 s55, s53, 0
	s_mov_b32 m0, s57
	s_nop 0
	global_load_lds_dwordx4 v215, s[54:55] offset:0
	s_nop 0
	s_mov_b32 m0, s58
	s_nop 0
	global_load_lds_dwordx4 v216, s[54:55] offset:0
	s_add_u32 s54, s51, 0x40100
	s_addc_u32 s55, s53, 0
	s_mov_b32 m0, s59
	s_nop 0
	global_load_lds_dwordx4 v215, s[54:55] offset:0
	s_nop 0
	s_mov_b32 m0, s60
	s_nop 0
	global_load_lds_dwordx4 v216, s[54:55] offset:0
	s_add_u32 s54, s47, 0x100
	s_addc_u32 s55, s50, 0
	s_mov_b32 m0, s56
	s_nop 0
	global_load_lds_dwordx4 v211, s[54:55] offset:0
	s_nop 0
	s_mov_b32 m0, s61
	s_nop 0
	global_load_lds_dwordx4 v213, s[54:55] offset:0
	s_cmp_lg_u32 s9, 0xfffffffe
	s_cbranch_scc1 .Lrope_skip
	s_lshl_b32 s100, s8, 14
	s_add_u32 s100, s96, s100
	s_addc_u32 s101, s97, 0
	s_mov_b32 m0, s98
	s_nop 0
	global_load_lds_dwordx4 v210, s[100:101] offset:0
	s_add_u32 s100, s100, 0x2000
	s_addc_u32 s101, s101, 0
	s_add_u32 s99, s98, 0x2000
	s_mov_b32 m0, s99
	s_nop 0
	global_load_lds_dwordx4 v210, s[100:101] offset:0
.Lrope_skip:
	s_waitcnt vmcnt(8)
	s_waitcnt lgkmcnt(0)
	s_barrier
	s_setprio 1
	s_waitcnt lgkmcnt(7)
	v_mfma_f32_16x16x32_bf16 v[62:65], v[130:133], v[162:165], v[62:65]
	v_mfma_f32_16x16x32_bf16 v[58:61], v[134:137], v[162:165], v[58:61]
	s_waitcnt lgkmcnt(6)
	v_mfma_f32_16x16x32_bf16 v[54:57], v[130:133], v[166:169], v[54:57]
	v_mfma_f32_16x16x32_bf16 v[50:53], v[134:137], v[166:169], v[50:53]
	s_waitcnt lgkmcnt(3)
	v_mfma_f32_16x16x32_bf16 v[46:49], v[130:133], v[178:181], v[46:49]
	v_mfma_f32_16x16x32_bf16 v[42:45], v[134:137], v[178:181], v[42:45]
	s_waitcnt lgkmcnt(2)
	v_mfma_f32_16x16x32_bf16 v[38:41], v[130:133], v[182:185], v[38:41]
	v_mfma_f32_16x16x32_bf16 v[34:37], v[134:137], v[182:185], v[34:37]
	v_mfma_f32_16x16x32_bf16 v[62:65], v[138:141], v[170:173], v[62:65]
	v_mfma_f32_16x16x32_bf16 v[58:61], v[142:145], v[170:173], v[58:61]
	v_mfma_f32_16x16x32_bf16 v[54:57], v[138:141], v[174:177], v[54:57]
	v_mfma_f32_16x16x32_bf16 v[50:53], v[142:145], v[174:177], v[50:53]
	s_waitcnt lgkmcnt(1)
	v_mfma_f32_16x16x32_bf16 v[46:49], v[138:141], v[186:189], v[46:49]
	v_mfma_f32_16x16x32_bf16 v[42:45], v[142:145], v[186:189], v[42:45]
	s_waitcnt lgkmcnt(0)
	v_mfma_f32_16x16x32_bf16 v[38:41], v[138:141], v[190:193], v[38:41]
	v_mfma_f32_16x16x32_bf16 v[34:37], v[142:145], v[190:193], v[34:37]
	s_setprio 0
	s_setprio 1
	v_mfma_f32_16x16x32_bf16 v[30:33], v[146:149], v[162:165], v[30:33]
	v_mfma_f32_16x16x32_bf16 v[26:29], v[150:153], v[162:165], v[26:29]
	v_mfma_f32_16x16x32_bf16 v[22:25], v[146:149], v[166:169], v[22:25]
	v_mfma_f32_16x16x32_bf16 v[18:21], v[150:153], v[166:169], v[18:21]
	v_mfma_f32_16x16x32_bf16 v[14:17], v[146:149], v[178:181], v[14:17]
	v_mfma_f32_16x16x32_bf16 v[10:13], v[150:153], v[178:181], v[10:13]
	v_mfma_f32_16x16x32_bf16 v[6:9], v[146:149], v[182:185], v[6:9]
	v_mfma_f32_16x16x32_bf16 v[2:5], v[150:153], v[182:185], v[2:5]
	v_mfma_f32_16x16x32_bf16 v[30:33], v[154:157], v[170:173], v[30:33]
	v_mfma_f32_16x16x32_bf16 v[26:29], v[158:161], v[170:173], v[26:29]
	v_mfma_f32_16x16x32_bf16 v[22:25], v[154:157], v[174:177], v[22:25]
	v_mfma_f32_16x16x32_bf16 v[18:21], v[158:161], v[174:177], v[18:21]
	v_mfma_f32_16x16x32_bf16 v[14:17], v[154:157], v[186:189], v[14:17]
	v_mfma_f32_16x16x32_bf16 v[10:13], v[158:161], v[186:189], v[10:13]
	v_mfma_f32_16x16x32_bf16 v[6:9], v[154:157], v[190:193], v[6:9]
	v_mfma_f32_16x16x32_bf16 v[2:5], v[158:161], v[190:193], v[2:5]
	s_setprio 0
	s_barrier
	s_add_i32 s78, 0, 0x18000
	v_add_u32_e32 v162, s78, v217
	v_add_u32_e32 v163, s78, v218
	s_add_i32 s78, 0, 0x1c000
	v_add_u32_e32 v164, s78, v217
	ds_read_b128 v[130:133], v162
	ds_read_b128 v[134:137], v162 offset:2048
	ds_read_b128 v[138:141], v163
	ds_read_b128 v[142:145], v163 offset:2048
	v_add_u32_e32 v165, s78, v218
	ds_read_b128 v[146:149], v164
	ds_read_b128 v[150:153], v164 offset:2048
	ds_read_b128 v[154:157], v165
	ds_read_b128 v[158:161], v165 offset:2048
	ds_read_b128 v[166:169], v223 offset:32768
	ds_read_b128 v[170:173], v223 offset:34816
	ds_read_b128 v[174:177], v224 offset:32768
	ds_read_b128 v[178:181], v224 offset:34816
	ds_read_b128 v[182:185], v223 offset:36864
	ds_read_b128 v[186:189], v223 offset:38912
	ds_read_b128 v[190:193], v224 offset:36864
	ds_read_b128 v[198:201], v224 offset:38912
	s_mov_b32 m0, s62
	s_nop 0
	global_load_lds_dwordx4 v212, s[54:55] offset:0
	s_nop 0
	s_mov_b32 m0, s63
	s_nop 0
	global_load_lds_dwordx4 v214, s[54:55] offset:0
	s_waitcnt vmcnt(8)
	s_waitcnt lgkmcnt(0)
	s_barrier
	s_setprio 1
	s_waitcnt lgkmcnt(7)
	v_mfma_f32_16x16x32_bf16 v[126:129], v[130:133], v[166:169], v[126:129]
	v_mfma_f32_16x16x32_bf16 v[122:125], v[134:137], v[166:169], v[122:125]
	s_waitcnt lgkmcnt(6)
	v_mfma_f32_16x16x32_bf16 v[118:121], v[130:133], v[170:173], v[118:121]
	v_mfma_f32_16x16x32_bf16 v[114:117], v[134:137], v[170:173], v[114:117]
	s_waitcnt lgkmcnt(3)
	v_mfma_f32_16x16x32_bf16 v[110:113], v[130:133], v[182:185], v[110:113]
	v_mfma_f32_16x16x32_bf16 v[106:109], v[134:137], v[182:185], v[106:109]
	s_waitcnt lgkmcnt(2)
	v_mfma_f32_16x16x32_bf16 v[102:105], v[130:133], v[186:189], v[102:105]
	v_mfma_f32_16x16x32_bf16 v[98:101], v[134:137], v[186:189], v[98:101]
	v_mfma_f32_16x16x32_bf16 v[126:129], v[138:141], v[174:177], v[126:129]
	v_mfma_f32_16x16x32_bf16 v[122:125], v[142:145], v[174:177], v[122:125]
	v_mfma_f32_16x16x32_bf16 v[118:121], v[138:141], v[178:181], v[118:121]
	v_mfma_f32_16x16x32_bf16 v[114:117], v[142:145], v[178:181], v[114:117]
	s_waitcnt lgkmcnt(1)
	v_mfma_f32_16x16x32_bf16 v[110:113], v[138:141], v[190:193], v[110:113]
	v_mfma_f32_16x16x32_bf16 v[106:109], v[142:145], v[190:193], v[106:109]
	s_waitcnt lgkmcnt(0)
	v_mfma_f32_16x16x32_bf16 v[102:105], v[138:141], v[198:201], v[102:105]
	v_mfma_f32_16x16x32_bf16 v[98:101], v[142:145], v[198:201], v[98:101]
	s_setprio 0
	s_setprio 1
	v_mfma_f32_16x16x32_bf16 v[94:97], v[146:149], v[166:169], v[94:97]
	v_mfma_f32_16x16x32_bf16 v[90:93], v[150:153], v[166:169], v[90:93]
	v_mfma_f32_16x16x32_bf16 v[86:89], v[146:149], v[170:173], v[86:89]
	v_mfma_f32_16x16x32_bf16 v[82:85], v[150:153], v[170:173], v[82:85]
	v_mfma_f32_16x16x32_bf16 v[78:81], v[146:149], v[182:185], v[78:81]
	v_mfma_f32_16x16x32_bf16 v[74:77], v[150:153], v[182:185], v[74:77]
	v_mfma_f32_16x16x32_bf16 v[70:73], v[146:149], v[186:189], v[70:73]
	v_mfma_f32_16x16x32_bf16 v[66:69], v[150:153], v[186:189], v[66:69]
	v_mfma_f32_16x16x32_bf16 v[94:97], v[154:157], v[174:177], v[94:97]
	v_mfma_f32_16x16x32_bf16 v[90:93], v[158:161], v[174:177], v[90:93]
	v_mfma_f32_16x16x32_bf16 v[86:89], v[154:157], v[178:181], v[86:89]
	v_mfma_f32_16x16x32_bf16 v[82:85], v[158:161], v[178:181], v[82:85]
	v_mfma_f32_16x16x32_bf16 v[78:81], v[154:157], v[190:193], v[78:81]
	v_mfma_f32_16x16x32_bf16 v[74:77], v[158:161], v[190:193], v[74:77]
	v_mfma_f32_16x16x32_bf16 v[70:73], v[154:157], v[198:201], v[70:73]
	v_mfma_f32_16x16x32_bf16 v[66:69], v[158:161], v[198:201], v[66:69]
	s_setprio 0
	s_barrier
	ds_read_b128 v[166:169], v223 offset:49152
	ds_read_b128 v[170:173], v223 offset:51200
	ds_read_b128 v[174:177], v224 offset:49152
	ds_read_b128 v[178:181], v224 offset:51200
	ds_read_b128 v[182:185], v223 offset:53248
	ds_read_b128 v[186:189], v223 offset:55296
	ds_read_b128 v[190:193], v224 offset:53248
	ds_read_b128 v[198:201], v224 offset:55296
	s_add_u32 s54, s51, 0x180
	s_addc_u32 s55, s53, 0
	s_mov_b32 m0, s64
	s_nop 0
	global_load_lds_dwordx4 v215, s[54:55] offset:0
	s_nop 0
	s_mov_b32 m0, s65
	s_nop 0
	global_load_lds_dwordx4 v216, s[54:55] offset:0
	s_add_u32 s54, s51, 0x40180
	s_addc_u32 s55, s53, 0
	s_mov_b32 m0, s68
	s_nop 0
	global_load_lds_dwordx4 v215, s[54:55] offset:0
	s_nop 0
	s_mov_b32 m0, s69
	s_nop 0
	global_load_lds_dwordx4 v216, s[54:55] offset:0
	s_add_u32 s54, s47, 0x180
	s_addc_u32 s55, s50, 0
	s_mov_b32 m0, s66
	s_nop 0
	global_load_lds_dwordx4 v211, s[54:55] offset:0
	s_nop 0
	s_mov_b32 m0, s67
	s_nop 0
	global_load_lds_dwordx4 v213, s[54:55] offset:0
	s_waitcnt vmcnt(8)
	s_waitcnt lgkmcnt(0)
	s_barrier
	s_setprio 1
	s_waitcnt lgkmcnt(7)
	v_mfma_f32_16x16x32_bf16 v[62:65], v[130:133], v[166:169], v[62:65]
	v_mfma_f32_16x16x32_bf16 v[58:61], v[134:137], v[166:169], v[58:61]
	s_waitcnt lgkmcnt(6)
	v_mfma_f32_16x16x32_bf16 v[54:57], v[130:133], v[170:173], v[54:57]
	v_mfma_f32_16x16x32_bf16 v[50:53], v[134:137], v[170:173], v[50:53]
	s_waitcnt lgkmcnt(3)
	v_mfma_f32_16x16x32_bf16 v[46:49], v[130:133], v[182:185], v[46:49]
	v_mfma_f32_16x16x32_bf16 v[42:45], v[134:137], v[182:185], v[42:45]
	s_waitcnt lgkmcnt(2)
	v_mfma_f32_16x16x32_bf16 v[38:41], v[130:133], v[186:189], v[38:41]
	v_mfma_f32_16x16x32_bf16 v[34:37], v[134:137], v[186:189], v[34:37]
	v_mfma_f32_16x16x32_bf16 v[62:65], v[138:141], v[174:177], v[62:65]
	v_mfma_f32_16x16x32_bf16 v[58:61], v[142:145], v[174:177], v[58:61]
	v_mfma_f32_16x16x32_bf16 v[54:57], v[138:141], v[178:181], v[54:57]
	v_mfma_f32_16x16x32_bf16 v[50:53], v[142:145], v[178:181], v[50:53]
	s_waitcnt lgkmcnt(1)
	v_mfma_f32_16x16x32_bf16 v[46:49], v[138:141], v[190:193], v[46:49]
	v_mfma_f32_16x16x32_bf16 v[42:45], v[142:145], v[190:193], v[42:45]
	s_waitcnt lgkmcnt(0)
	v_mfma_f32_16x16x32_bf16 v[38:41], v[138:141], v[198:201], v[38:41]
	v_mfma_f32_16x16x32_bf16 v[34:37], v[142:145], v[198:201], v[34:37]
	s_setprio 0
	s_setprio 1
	v_mfma_f32_16x16x32_bf16 v[30:33], v[146:149], v[166:169], v[30:33]
	v_mfma_f32_16x16x32_bf16 v[26:29], v[150:153], v[166:169], v[26:29]
	v_mfma_f32_16x16x32_bf16 v[22:25], v[146:149], v[170:173], v[22:25]
	v_mfma_f32_16x16x32_bf16 v[18:21], v[150:153], v[170:173], v[18:21]
	v_mfma_f32_16x16x32_bf16 v[14:17], v[146:149], v[182:185], v[14:17]
	v_mfma_f32_16x16x32_bf16 v[10:13], v[150:153], v[182:185], v[10:13]
	v_mfma_f32_16x16x32_bf16 v[6:9], v[146:149], v[186:189], v[6:9]
	v_mfma_f32_16x16x32_bf16 v[2:5], v[150:153], v[186:189], v[2:5]
	v_mfma_f32_16x16x32_bf16 v[30:33], v[154:157], v[174:177], v[30:33]
	v_mfma_f32_16x16x32_bf16 v[26:29], v[158:161], v[174:177], v[26:29]
	v_mfma_f32_16x16x32_bf16 v[22:25], v[154:157], v[178:181], v[22:25]
	v_mfma_f32_16x16x32_bf16 v[18:21], v[158:161], v[178:181], v[18:21]
	v_mfma_f32_16x16x32_bf16 v[14:17], v[154:157], v[190:193], v[14:17]
	v_mfma_f32_16x16x32_bf16 v[10:13], v[158:161], v[190:193], v[10:13]
	v_mfma_f32_16x16x32_bf16 v[6:9], v[154:157], v[198:201], v[6:9]
	v_mfma_f32_16x16x32_bf16 v[2:5], v[158:161], v[198:201], v[2:5]
	s_setprio 0
	s_barrier
	s_add_i32 s9, s9, 2
	s_add_u32 s4, s4, 0x100
	s_addc_u32 s5, s5, 0
	s_cmp_lt_u32 s9, 12
	s_cbranch_scc1 .LBB0_126
	ds_read_b128 v[146:149], v219
	ds_read_b128 v[150:153], v219 offset:2048
	ds_read_b128 v[158:161], v220
	ds_read_b128 v[154:157], v220 offset:2048
	ds_read_b128 v[130:133], v221
	ds_read_b128 v[134:137], v221 offset:2048
	ds_read_b128 v[142:145], v222
	ds_read_b128 v[138:141], v222 offset:2048
	ds_read_b128 v[166:169], v223
	ds_read_b128 v[170:173], v223 offset:2048
	ds_read_b128 v[174:177], v224
	ds_read_b128 v[178:181], v224 offset:2048
	ds_read_b128 v[182:185], v223 offset:4096
	ds_read_b128 v[186:189], v223 offset:6144
	ds_read_b128 v[190:193], v224 offset:4096
	ds_read_b128 v[198:201], v224 offset:6144
	s_mov_b32 m0, s70
	s_nop 0
	global_load_lds_dwordx4 v212, s[24:25] offset:0
	s_nop 0
	s_mov_b32 m0, s71
	s_nop 0
	global_load_lds_dwordx4 v214, s[24:25] offset:0
	s_waitcnt vmcnt(8)
	s_waitcnt lgkmcnt(0)
	s_barrier
	s_setprio 1
	s_waitcnt lgkmcnt(7)
	v_mfma_f32_16x16x32_bf16 v[126:129], v[146:149], v[166:169], v[126:129]
	v_mfma_f32_16x16x32_bf16 v[122:125], v[150:153], v[166:169], v[122:125]
	s_waitcnt lgkmcnt(6)
	v_mfma_f32_16x16x32_bf16 v[118:121], v[146:149], v[170:173], v[118:121]
	v_mfma_f32_16x16x32_bf16 v[114:117], v[150:153], v[170:173], v[114:117]
	s_waitcnt lgkmcnt(3)
	v_mfma_f32_16x16x32_bf16 v[110:113], v[146:149], v[182:185], v[110:113]
	v_mfma_f32_16x16x32_bf16 v[106:109], v[150:153], v[182:185], v[106:109]
	s_waitcnt lgkmcnt(2)
	v_mfma_f32_16x16x32_bf16 v[102:105], v[146:149], v[186:189], v[102:105]
	v_mfma_f32_16x16x32_bf16 v[98:101], v[150:153], v[186:189], v[98:101]
	v_mfma_f32_16x16x32_bf16 v[126:129], v[158:161], v[174:177], v[126:129]
	v_mfma_f32_16x16x32_bf16 v[122:125], v[154:157], v[174:177], v[122:125]
	v_mfma_f32_16x16x32_bf16 v[118:121], v[158:161], v[178:181], v[118:121]
	v_mfma_f32_16x16x32_bf16 v[114:117], v[154:157], v[178:181], v[114:117]
	s_waitcnt lgkmcnt(1)
	v_mfma_f32_16x16x32_bf16 v[110:113], v[158:161], v[190:193], v[110:113]
	v_mfma_f32_16x16x32_bf16 v[106:109], v[154:157], v[190:193], v[106:109]
	s_waitcnt lgkmcnt(0)
	v_mfma_f32_16x16x32_bf16 v[102:105], v[158:161], v[198:201], v[102:105]
	v_mfma_f32_16x16x32_bf16 v[98:101], v[154:157], v[198:201], v[98:101]
	s_setprio 0
	s_setprio 1
	v_mfma_f32_16x16x32_bf16 v[94:97], v[130:133], v[166:169], v[94:97]
	v_mfma_f32_16x16x32_bf16 v[90:93], v[134:137], v[166:169], v[90:93]
	v_mfma_f32_16x16x32_bf16 v[86:89], v[130:133], v[170:173], v[86:89]
	v_mfma_f32_16x16x32_bf16 v[82:85], v[134:137], v[170:173], v[82:85]
	v_mfma_f32_16x16x32_bf16 v[78:81], v[130:133], v[182:185], v[78:81]
	v_mfma_f32_16x16x32_bf16 v[74:77], v[134:137], v[182:185], v[74:77]
	v_mfma_f32_16x16x32_bf16 v[70:73], v[130:133], v[186:189], v[70:73]
	v_mfma_f32_16x16x32_bf16 v[66:69], v[134:137], v[186:189], v[66:69]
	v_mfma_f32_16x16x32_bf16 v[94:97], v[142:145], v[174:177], v[94:97]
	v_mfma_f32_16x16x32_bf16 v[90:93], v[138:141], v[174:177], v[90:93]
	v_mfma_f32_16x16x32_bf16 v[86:89], v[142:145], v[178:181], v[86:89]
	v_mfma_f32_16x16x32_bf16 v[82:85], v[138:141], v[178:181], v[82:85]
	v_mfma_f32_16x16x32_bf16 v[78:81], v[142:145], v[190:193], v[78:81]
	v_mfma_f32_16x16x32_bf16 v[74:77], v[138:141], v[190:193], v[74:77]
	v_mfma_f32_16x16x32_bf16 v[70:73], v[142:145], v[198:201], v[70:73]
	v_mfma_f32_16x16x32_bf16 v[66:69], v[138:141], v[198:201], v[66:69]
	s_setprio 0
	s_barrier
	v_cndmask_b32_e64 v166, 0, 1, s[6:7]
	v_cmp_ne_u32_e64 s[4:5], 1, v166
	s_andn2_b64 vcc, exec, s[6:7]
	s_cbranch_vccnz .LBB0_129
	v_mov_b32_e32 v166, v0
	s_nop 0
	v_lshlrev_b32_e32 v167, 4, v166
	v_bitop3_b32 v167, v167, s2, v166 bitop3:0x48
	v_lshlrev_b32_e32 v166, 8, v166
	v_lshl_or_b32 v167, s48, 19, v167
	v_and_b32_e32 v166, 0xfffff800, v166
	v_add_u32_e32 v211, v167, v166
	v_add_u32_e32 v212, 0x40000, v211
	v_add_u32_e32 v213, 0x20000, v211
	v_add_u32_e32 v214, 0x60000, v211

.LBB0_131:
	v_mov_b32_e32 v227, v0
	s_cmp_lt_i32 s52, 4
	v_ashrrev_i32_e32 v26, 2, v227
	v_and_b32_e32 v201, 0xffffffc0, v26
	v_and_b32_e32 v200, 15, v227
	v_bfe_u32 v228, v227, 4, 2
	v_lshl_add_u32 v26, s8, 8, v201
	v_or_b32_e32 v198, v26, v200
	s_cselect_b64 s[54:55], -1, 0
	s_cmp_gt_i32 s52, 3
	v_cmp_gt_u32_e64 s[6:7], 2, v228
	s_cbranch_scc1 .LBB0_135
	s_and_saveexec_b64 s[8:9], s[6:7]
	s_cbranch_execz .LBB0_134
	v_ashrrev_i32_e32 v199, 31, v198
	v_lshlrev_b64 v[26:27], 6, v[198:199]
	v_lshl_add_u64 v[26:27], s[20:21], 0, v[26:27]
	ds_read_b128 v[118:121], v255 offset:48
	ds_read_b128 v[126:129], v255 offset:32
	ds_read_b128 v[114:117], v255 offset:16
	ds_read_b128 v[122:125], v255 offset:0
	v_or_b32_e32 v26, 16, v198
	v_ashrrev_i32_e32 v27, 31, v26
	v_lshlrev_b64 v[26:27], 6, v[26:27]
	v_lshl_add_u64 v[26:27], s[20:21], 0, v[26:27]
	ds_read_b128 v[86:89], v255 offset:1072
	ds_read_b128 v[94:97], v255 offset:1056
	ds_read_b128 v[194:197], v255 offset:1040
	ds_read_b128 v[230:233], v255 offset:1024
	v_or_b32_e32 v26, 32, v198
	v_ashrrev_i32_e32 v27, 31, v26
	v_lshlrev_b64 v[26:27], 6, v[26:27]
	v_lshl_add_u64 v[26:27], s[20:21], 0, v[26:27]
	ds_read_b128 v[66:69], v255 offset:2096
	ds_read_b128 v[70:73], v255 offset:2080
	ds_read_b128 v[58:61], v255 offset:2064
	ds_read_b128 v[62:65], v255 offset:2048
	v_or_b32_e32 v26, 48, v198
	v_ashrrev_i32_e32 v27, 31, v26
	v_lshlrev_b64 v[26:27], 6, v[26:27]
	v_lshl_add_u64 v[42:43], s[20:21], 0, v[26:27]
	ds_read_b128 v[34:37], v255 offset:3120
	ds_read_b128 v[46:49], v255 offset:3104
	ds_read_b128 v[26:29], v255 offset:3088
	s_nop 0
	ds_read_b128 v[42:45], v255 offset:3072
	s_waitcnt lgkmcnt(0)

.LBB0_135:
	s_lshl_b32 s8, s49, 10
	s_and_b32 s8, s8, 0x400
	s_add_i32 s8, s8, 0
	s_add_i32 s8, s8, 0x24cc0
	v_lshlrev_b32_e32 v138, 2, v201
	v_lshlrev_b32_e32 v139, 2, v200
	v_add3_u32 v226, s8, v138, v139
	ds_read_b32 v200, v226
	v_cndmask_b32_e64 v138, 0, 1, s[54:55]
	v_cmp_eq_u32_e64 s[8:9], 0, v228
	v_cmp_ne_u32_e64 s[10:11], 1, v138
	s_andn2_b64 vcc, exec, s[54:55]
	s_waitcnt lgkmcnt(0)
	v_pk_mul_f32 v[192:193], v[192:193], v[200:201] op_sel_hi:[1,0]
	v_pk_mul_f32 v[190:191], v[190:191], v[200:201] op_sel_hi:[1,0]
	v_pk_mul_f32 v[188:189], v[188:189], v[200:201] op_sel_hi:[1,0]
	v_pk_mul_f32 v[202:203], v[186:187], v[200:201] op_sel_hi:[1,0]
	s_cbranch_vccnz .LBB0_139
	v_and_b32_e32 v139, 64, v225
	v_xor_b32_e32 v138, 16, v225
	v_add_u32_e32 v139, 64, v139
	v_cmp_lt_i32_e32 vcc, v138, v139
	s_nop 1
	v_cndmask_b32_e32 v138, v225, v138, vcc
	v_lshlrev_b32_e32 v138, 2, v138
	ds_bpermute_b32 v208, v138, v190
	ds_bpermute_b32 v204, v138, v202
	ds_bpermute_b32 v209, v138, v191
	ds_bpermute_b32 v205, v138, v203
	ds_bpermute_b32 v206, v138, v192
	ds_bpermute_b32 v186, v138, v188
	ds_bpermute_b32 v207, v138, v193
	ds_bpermute_b32 v187, v138, v189
	s_and_saveexec_b64 s[54:55], s[6:7]
	s_cbranch_execz .LBB0_138
	v_xor_b32_e32 v140, 0x80000000, v126
	v_xor_b32_e32 v141, 0x80000000, v127
	v_xor_b32_e32 v138, 0x80000000, v128
	v_xor_b32_e32 v139, 0x80000000, v129
	v_cndmask_b32_e64 v139, v129, v139, s[8:9]
	v_cndmask_b32_e64 v138, v128, v138, s[8:9]
	v_cndmask_b32_e64 v141, v127, v141, s[8:9]
	v_cndmask_b32_e64 v140, v126, v140, s[8:9]
	s_waitcnt lgkmcnt(5)
	v_pk_mul_f32 v[140:141], v[140:141], v[208:209]
	s_waitcnt lgkmcnt(1)
	v_pk_mul_f32 v[138:139], v[138:139], v[206:207]
	v_pk_fma_f32 v[190:191], v[122:123], v[190:191], v[140:141]
	v_pk_fma_f32 v[192:193], v[124:125], v[192:193], v[138:139]
	v_xor_b32_e32 v140, 0x80000000, v118
	v_xor_b32_e32 v141, 0x80000000, v119
	v_xor_b32_e32 v138, 0x80000000, v120
	v_xor_b32_e32 v139, 0x80000000, v121
	v_cndmask_b32_e64 v139, v121, v139, s[8:9]
	v_cndmask_b32_e64 v138, v120, v138, s[8:9]
	v_cndmask_b32_e64 v141, v119, v141, s[8:9]
	v_cndmask_b32_e64 v140, v118, v140, s[8:9]
	v_pk_mul_f32 v[140:141], v[140:141], v[204:205]
	s_waitcnt lgkmcnt(0)
	v_pk_mul_f32 v[138:139], v[138:139], v[186:187]
	v_pk_fma_f32 v[202:203], v[114:115], v[202:203], v[140:141]
	v_pk_fma_f32 v[188:189], v[116:117], v[188:189], v[138:139]

.LBB0_139:
	v_and_b32_e32 v138, 0xc0, v227
	v_lshl_or_b32 v138, s52, 8, v138
	v_mov_b32_e32 v201, v200
	s_waitcnt lgkmcnt(2)
	v_lshl_or_b32 v186, v228, 3, v138
	v_mov_b32_e32 v138, v200
	v_mov_b32_e32 v139, v200
	v_pk_mul_f32 v[144:145], v[184:185], v[138:139]
	v_pk_mul_f32 v[142:143], v[182:183], v[200:201]
	v_pk_mul_f32 v[178:179], v[178:179], v[200:201]
	v_pk_mul_f32 v[180:181], v[180:181], v[138:139]
	v_cvt_pk_bf16_f32 v138, v190, v191
	v_cvt_pk_bf16_f32 v139, v192, v193
	v_cvt_pk_bf16_f32 v140, v202, v203
	v_cvt_pk_bf16_f32 v141, v188, v189
	v_cvt_pk_bf16_f32 v142, v142, v143
	v_cvt_pk_bf16_f32 v143, v144, v145
	v_cvt_pk_bf16_f32 v144, v178, v179
	s_nop 0
	v_cvt_pk_bf16_f32 v145, v180, v181
	ds_read_b32 v178, v226 offset:64
	v_ashrrev_i32_e32 v199, 31, v198
	v_lshlrev_b64 v[204:205], 12, v[198:199]
	s_waitcnt lgkmcnt(1)
	v_ashrrev_i32_e32 v187, 31, v186
	v_lshl_add_u64 v[180:181], s[18:19], 0, v[204:205]
	v_lshl_add_u64 v[180:181], v[186:187], 1, v[180:181]
	s_waitcnt lgkmcnt(0)
	v_pk_mul_f32 v[176:177], v[176:177], v[178:179] op_sel_hi:[1,0]
	v_pk_mul_f32 v[174:175], v[174:175], v[178:179] op_sel_hi:[1,0]
	v_pk_mul_f32 v[172:173], v[172:173], v[178:179] op_sel_hi:[1,0]
	s_and_b64 vcc, exec, s[10:11]
	v_pk_mul_f32 v[170:171], v[170:171], v[178:179] op_sel_hi:[1,0]
	global_store_dwordx4 v[180:181], v[138:141], off
	global_store_dwordx4 v[180:181], v[142:145], off offset:64
	s_cbranch_vccnz .LBB0_143
	v_and_b32_e32 v139, 64, v225
	v_xor_b32_e32 v138, 16, v225
	v_add_u32_e32 v139, 64, v139
	v_cmp_lt_i32_e32 vcc, v138, v139
	s_nop 1
	v_cndmask_b32_e32 v138, v225, v138, vcc
	v_lshlrev_b32_e32 v138, 2, v138
	ds_bpermute_b32 v188, v138, v174
	ds_bpermute_b32 v182, v138, v170
	ds_bpermute_b32 v189, v138, v175
	ds_bpermute_b32 v183, v138, v171
	ds_bpermute_b32 v184, v138, v176
	ds_bpermute_b32 v180, v138, v172
	ds_bpermute_b32 v185, v138, v177
	ds_bpermute_b32 v181, v138, v173
	s_and_saveexec_b64 s[52:53], s[6:7]
	s_cbranch_execz .LBB0_142
	v_xor_b32_e32 v140, 0x80000000, v94
	v_xor_b32_e32 v141, 0x80000000, v95
	v_xor_b32_e32 v138, 0x80000000, v96
	v_xor_b32_e32 v139, 0x80000000, v97
	v_cndmask_b32_e64 v139, v97, v139, s[8:9]
	v_cndmask_b32_e64 v138, v96, v138, s[8:9]
	v_cndmask_b32_e64 v141, v95, v141, s[8:9]
	v_cndmask_b32_e64 v140, v94, v140, s[8:9]
	s_waitcnt lgkmcnt(5)
	v_pk_mul_f32 v[140:141], v[140:141], v[188:189]
	s_waitcnt lgkmcnt(1)
	v_pk_mul_f32 v[138:139], v[138:139], v[184:185]
	v_pk_fma_f32 v[174:175], v[230:231], v[174:175], v[140:141]
	v_pk_fma_f32 v[176:177], v[232:233], v[176:177], v[138:139]
	v_xor_b32_e32 v140, 0x80000000, v86
	v_xor_b32_e32 v141, 0x80000000, v87
	v_xor_b32_e32 v138, 0x80000000, v88
	v_xor_b32_e32 v139, 0x80000000, v89
	v_cndmask_b32_e64 v139, v89, v139, s[8:9]
	v_cndmask_b32_e64 v138, v88, v138, s[8:9]
	v_cndmask_b32_e64 v141, v87, v141, s[8:9]
	v_cndmask_b32_e64 v140, v86, v140, s[8:9]
	v_pk_mul_f32 v[140:141], v[140:141], v[182:183]
	s_waitcnt lgkmcnt(0)
	v_pk_mul_f32 v[138:139], v[138:139], v[180:181]
	v_pk_fma_f32 v[170:171], v[194:195], v[170:171], v[140:141]
	v_pk_fma_f32 v[172:173], v[196:197], v[172:173], v[138:139]

.LBB0_143:
	v_or_b32_e32 v138, 16, v198
	v_ashrrev_i32_e32 v139, 31, v138
	v_mov_b32_e32 v179, v178
	s_waitcnt lgkmcnt(0)
	v_lshlrev_b64 v[180:181], 12, v[138:139]
	v_mov_b32_e32 v138, v178
	v_mov_b32_e32 v139, v178
	v_pk_mul_f32 v[144:145], v[168:169], v[138:139]
	v_pk_mul_f32 v[142:143], v[166:167], v[178:179]
	v_pk_mul_f32 v[162:163], v[162:163], v[178:179]
	v_pk_mul_f32 v[164:165], v[164:165], v[138:139]
	v_cvt_pk_bf16_f32 v138, v174, v175
	v_cvt_pk_bf16_f32 v139, v176, v177
	v_cvt_pk_bf16_f32 v140, v170, v171
	v_cvt_pk_bf16_f32 v141, v172, v173
	v_cvt_pk_bf16_f32 v142, v142, v143
	v_cvt_pk_bf16_f32 v143, v144, v145
	v_cvt_pk_bf16_f32 v144, v162, v163
	s_nop 0
	v_cvt_pk_bf16_f32 v145, v164, v165
	ds_read_b32 v162, v226 offset:128
	v_lshl_add_u64 v[164:165], s[18:19], 0, v[180:181]
	v_lshl_add_u64 v[164:165], v[186:187], 1, v[164:165]
	s_and_b64 vcc, exec, s[10:11]
	global_store_dwordx4 v[164:165], v[138:141], off
	global_store_dwordx4 v[164:165], v[142:145], off offset:64
	s_waitcnt lgkmcnt(0)
	v_pk_mul_f32 v[160:161], v[160:161], v[162:163] op_sel_hi:[1,0]
	v_pk_mul_f32 v[158:159], v[158:159], v[162:163] op_sel_hi:[1,0]
	v_pk_mul_f32 v[156:157], v[156:157], v[162:163] op_sel_hi:[1,0]
	v_pk_mul_f32 v[154:155], v[154:155], v[162:163] op_sel_hi:[1,0]
	s_cbranch_vccnz .LBB0_147
	v_and_b32_e32 v139, 64, v225
	v_xor_b32_e32 v138, 16, v225
	v_add_u32_e32 v139, 64, v139
	v_cmp_lt_i32_e32 vcc, v138, v139
	s_nop 1
	v_cndmask_b32_e32 v138, v225, v138, vcc
	v_lshlrev_b32_e32 v138, 2, v138
	ds_bpermute_b32 v170, v138, v158
	ds_bpermute_b32 v166, v138, v154
	ds_bpermute_b32 v171, v138, v159
	ds_bpermute_b32 v167, v138, v155
	ds_bpermute_b32 v168, v138, v160
	ds_bpermute_b32 v164, v138, v156
	ds_bpermute_b32 v169, v138, v161
	ds_bpermute_b32 v165, v138, v157
	s_and_saveexec_b64 s[52:53], s[6:7]
	s_cbranch_execz .LBB0_146
	v_xor_b32_e32 v140, 0x80000000, v70
	v_xor_b32_e32 v141, 0x80000000, v71
	v_xor_b32_e32 v138, 0x80000000, v72
	v_xor_b32_e32 v139, 0x80000000, v73
	v_cndmask_b32_e64 v139, v73, v139, s[8:9]
	v_cndmask_b32_e64 v138, v72, v138, s[8:9]
	v_cndmask_b32_e64 v141, v71, v141, s[8:9]
	v_cndmask_b32_e64 v140, v70, v140, s[8:9]
	s_waitcnt lgkmcnt(5)
	v_pk_mul_f32 v[140:141], v[140:141], v[170:171]
	s_waitcnt lgkmcnt(1)
	v_pk_mul_f32 v[138:139], v[138:139], v[168:169]
	v_pk_fma_f32 v[158:159], v[62:63], v[158:159], v[140:141]
	v_pk_fma_f32 v[160:161], v[64:65], v[160:161], v[138:139]
	v_xor_b32_e32 v140, 0x80000000, v66
	v_xor_b32_e32 v141, 0x80000000, v67
	v_xor_b32_e32 v138, 0x80000000, v68
	v_xor_b32_e32 v139, 0x80000000, v69
	v_cndmask_b32_e64 v139, v69, v139, s[8:9]
	v_cndmask_b32_e64 v138, v68, v138, s[8:9]
	v_cndmask_b32_e64 v141, v67, v141, s[8:9]
	v_cndmask_b32_e64 v140, v66, v140, s[8:9]
	v_pk_mul_f32 v[140:141], v[140:141], v[166:167]
	s_waitcnt lgkmcnt(0)
	v_pk_mul_f32 v[138:139], v[138:139], v[164:165]
	v_pk_fma_f32 v[154:155], v[58:59], v[154:155], v[140:141]
	v_pk_fma_f32 v[156:157], v[60:61], v[156:157], v[138:139]

.LBB0_147:
	v_or_b32_e32 v138, 32, v198
	v_ashrrev_i32_e32 v139, 31, v138
	v_mov_b32_e32 v163, v162
	s_waitcnt lgkmcnt(0)
	v_lshlrev_b64 v[164:165], 12, v[138:139]
	v_mov_b32_e32 v138, v162
	v_mov_b32_e32 v139, v162
	v_pk_mul_f32 v[144:145], v[152:153], v[138:139]
	v_pk_mul_f32 v[142:143], v[150:151], v[162:163]
	v_pk_mul_f32 v[146:147], v[146:147], v[162:163]
	v_pk_mul_f32 v[148:149], v[148:149], v[138:139]
	v_cvt_pk_bf16_f32 v138, v158, v159
	v_cvt_pk_bf16_f32 v139, v160, v161
	v_cvt_pk_bf16_f32 v140, v154, v155
	v_cvt_pk_bf16_f32 v141, v156, v157
	v_cvt_pk_bf16_f32 v142, v142, v143
	v_cvt_pk_bf16_f32 v143, v144, v145
	v_cvt_pk_bf16_f32 v144, v146, v147
	s_nop 0
	v_cvt_pk_bf16_f32 v145, v148, v149
	ds_read_b32 v146, v226 offset:192
	v_lshl_add_u64 v[148:149], s[18:19], 0, v[164:165]
	v_lshl_add_u64 v[148:149], v[186:187], 1, v[148:149]
	global_store_dwordx4 v[148:149], v[138:141], off
	global_store_dwordx4 v[148:149], v[142:145], off offset:64
	s_and_b64 vcc, exec, s[10:11]
	s_waitcnt lgkmcnt(0)
	v_pk_mul_f32 v[140:141], v[100:101], v[146:147] op_sel_hi:[1,0]
	v_pk_mul_f32 v[144:145], v[104:105], v[146:147] op_sel_hi:[1,0]
	v_pk_mul_f32 v[142:143], v[102:103], v[146:147] op_sel_hi:[1,0]
	v_pk_mul_f32 v[138:139], v[98:99], v[146:147] op_sel_hi:[1,0]
	s_cbranch_vccnz .LBB0_151
	v_and_b32_e32 v99, 64, v225
	v_xor_b32_e32 v98, 16, v225
	v_add_u32_e32 v99, 64, v99
	v_cmp_lt_i32_e32 vcc, v98, v99
	s_nop 1
	v_cndmask_b32_e32 v98, v225, v98, vcc
	v_lshlrev_b32_e32 v98, 2, v98
	ds_bpermute_b32 v154, v98, v142
	ds_bpermute_b32 v150, v98, v138
	ds_bpermute_b32 v155, v98, v143
	ds_bpermute_b32 v151, v98, v139
	ds_bpermute_b32 v152, v98, v144
	ds_bpermute_b32 v148, v98, v140
	ds_bpermute_b32 v153, v98, v145
	ds_bpermute_b32 v149, v98, v141
	s_and_saveexec_b64 s[52:53], s[6:7]
	s_cbranch_execz .LBB0_150
	v_xor_b32_e32 v100, 0x80000000, v46
	v_xor_b32_e32 v101, 0x80000000, v47
	v_xor_b32_e32 v98, 0x80000000, v48
	v_xor_b32_e32 v99, 0x80000000, v49
	v_cndmask_b32_e64 v99, v49, v99, s[8:9]
	v_cndmask_b32_e64 v98, v48, v98, s[8:9]
	v_cndmask_b32_e64 v101, v47, v101, s[8:9]
	v_cndmask_b32_e64 v100, v46, v100, s[8:9]
	s_waitcnt lgkmcnt(5)
	v_pk_mul_f32 v[100:101], v[100:101], v[154:155]
	s_waitcnt lgkmcnt(1)
	v_pk_mul_f32 v[98:99], v[98:99], v[152:153]
	v_pk_fma_f32 v[142:143], v[42:43], v[142:143], v[100:101]
	v_pk_fma_f32 v[144:145], v[44:45], v[144:145], v[98:99]
	v_xor_b32_e32 v100, 0x80000000, v34
	v_xor_b32_e32 v101, 0x80000000, v35
	v_xor_b32_e32 v98, 0x80000000, v36
	v_xor_b32_e32 v99, 0x80000000, v37
	v_cndmask_b32_e64 v99, v37, v99, s[8:9]
	v_cndmask_b32_e64 v98, v36, v98, s[8:9]
	v_cndmask_b32_e64 v101, v35, v101, s[8:9]
	v_cndmask_b32_e64 v100, v34, v100, s[8:9]
	v_pk_mul_f32 v[100:101], v[100:101], v[150:151]
	s_waitcnt lgkmcnt(0)
	v_pk_mul_f32 v[98:99], v[98:99], v[148:149]
	v_pk_fma_f32 v[138:139], v[26:27], v[138:139], v[100:101]
	v_pk_fma_f32 v[140:141], v[28:29], v[140:141], v[98:99]

.LBB0_151:
	v_or_b32_e32 v98, 48, v198
	v_ashrrev_i32_e32 v99, 31, v98
	v_lshlrev_b64 v[98:99], 12, v[98:99]
	v_lshl_add_u64 v[98:99], s[18:19], 0, v[98:99]
	v_mov_b32_e32 v147, v146
	s_waitcnt lgkmcnt(0)
	v_lshl_add_u64 v[148:149], v[186:187], 1, v[98:99]
	v_mov_b32_e32 v98, v146
	v_mov_b32_e32 v99, v146
	v_pk_mul_f32 v[104:105], v[136:137], v[98:99]
	v_pk_mul_f32 v[102:103], v[134:135], v[146:147]
	s_and_b64 vcc, exec, s[10:11]
	v_pk_mul_f32 v[132:133], v[132:133], v[98:99]
	v_pk_mul_f32 v[130:131], v[130:131], v[146:147]
	v_cvt_pk_bf16_f32 v98, v142, v143
	v_cvt_pk_bf16_f32 v99, v144, v145
	v_cvt_pk_bf16_f32 v100, v138, v139
	v_cvt_pk_bf16_f32 v101, v140, v141
	v_cvt_pk_bf16_f32 v102, v102, v103
	v_cvt_pk_bf16_f32 v103, v104, v105
	s_nop 0
	v_cvt_pk_bf16_f32 v104, v130, v131
	v_cvt_pk_bf16_f32 v105, v132, v133
	global_store_dwordx4 v[148:149], v[98:101], off
	global_store_dwordx4 v[148:149], v[102:105], off offset:64
	s_cbranch_vccnz .LBB0_155
	s_and_saveexec_b64 s[52:53], s[6:7]
	s_cbranch_execz .LBB0_154
	v_lshlrev_b64 v[26:27], 6, v[198:199]
	v_lshl_add_u64 v[26:27], s[20:21], 0, v[26:27]
	v_add_co_u32_e32 v34, vcc, 0x2000, v26
	v_lshl_add_u64 v[28:29], v[26:27], 0, s[28:29]
	s_nop 0
	v_addc_co_u32_e32 v35, vcc, 0, v27, vcc
	ds_read_b128 v[122:125], v255 offset:8192
	ds_read_b128 v[118:121], v255 offset:8240
	ds_read_b128 v[126:129], v255 offset:8224
	ds_read_b128 v[114:117], v255 offset:8208
	v_lshl_add_u64 v[28:29], v[26:27], 0, s[30:31]
	v_lshl_add_u64 v[66:67], v[26:27], 0, s[34:35]
	v_lshl_add_u64 v[26:27], v[26:27], 0, s[36:37]
	ds_read_b128 v[86:89], v255 offset:9264
	ds_read_b128 v[94:97], v255 offset:9248
	ds_read_b128 v[230:233], v255 offset:9216
	ds_read_b128 v[62:65], v255 offset:10240
	ds_read_b128 v[70:73], v255 offset:10272
	ds_read_b128 v[58:61], v255 offset:10256
	ds_read_b128 v[194:197], v255 offset:9232
	ds_read_b128 v[42:45], v255 offset:11264
	s_nop 0
	ds_read_b128 v[34:37], v255 offset:11312
	ds_read_b128 v[46:49], v255 offset:11296
	s_nop 0
	ds_read_b128 v[66:69], v255 offset:10288
	s_nop 0
	ds_read_b128 v[26:29], v255 offset:11280
	s_waitcnt lgkmcnt(0)

.LBB0_155:
	ds_read_b32 v130, v226 offset:512
	s_and_b64 vcc, exec, s[10:11]
	s_waitcnt lgkmcnt(0)
	v_pk_mul_f32 v[132:133], v[108:109], v[130:131] op_sel_hi:[1,0]
	v_pk_mul_f32 v[134:135], v[106:107], v[130:131] op_sel_hi:[1,0]
	v_pk_mul_f32 v[108:109], v[112:113], v[130:131] op_sel_hi:[1,0]
	v_pk_mul_f32 v[110:111], v[110:111], v[130:131] op_sel_hi:[1,0]
	s_cbranch_vccnz .LBB0_159
	v_and_b32_e32 v99, 64, v225
	v_xor_b32_e32 v98, 16, v225
	v_add_u32_e32 v99, 64, v99
	v_cmp_lt_i32_e32 vcc, v98, v99
	s_nop 1
	v_cndmask_b32_e32 v98, v225, v98, vcc
	v_lshlrev_b32_e32 v98, 2, v98
	ds_bpermute_b32 v138, v98, v134
	ds_bpermute_b32 v112, v98, v110
	ds_bpermute_b32 v139, v98, v135
	ds_bpermute_b32 v113, v98, v111
	ds_bpermute_b32 v136, v98, v132
	ds_bpermute_b32 v106, v98, v108
	ds_bpermute_b32 v137, v98, v133
	ds_bpermute_b32 v107, v98, v109
	s_and_saveexec_b64 s[52:53], s[6:7]
	s_cbranch_execz .LBB0_158
	v_xor_b32_e32 v100, 0x80000000, v126
	v_xor_b32_e32 v101, 0x80000000, v127
	v_xor_b32_e32 v98, 0x80000000, v128
	v_xor_b32_e32 v99, 0x80000000, v129
	v_cndmask_b32_e64 v99, v129, v99, s[8:9]
	v_cndmask_b32_e64 v98, v128, v98, s[8:9]
	v_cndmask_b32_e64 v101, v127, v101, s[8:9]
	v_cndmask_b32_e64 v100, v126, v100, s[8:9]
	s_waitcnt lgkmcnt(5)
	v_pk_mul_f32 v[100:101], v[100:101], v[138:139]
	s_waitcnt lgkmcnt(1)
	v_pk_mul_f32 v[98:99], v[98:99], v[136:137]
	v_pk_fma_f32 v[134:135], v[122:123], v[134:135], v[100:101]
	v_pk_fma_f32 v[132:133], v[124:125], v[132:133], v[98:99]
	v_xor_b32_e32 v100, 0x80000000, v118
	v_xor_b32_e32 v101, 0x80000000, v119
	v_xor_b32_e32 v98, 0x80000000, v120
	v_xor_b32_e32 v99, 0x80000000, v121
	v_cndmask_b32_e64 v99, v121, v99, s[8:9]
	v_cndmask_b32_e64 v98, v120, v98, s[8:9]
	v_cndmask_b32_e64 v101, v119, v101, s[8:9]
	v_cndmask_b32_e64 v100, v118, v100, s[8:9]
	v_pk_mul_f32 v[100:101], v[100:101], v[112:113]
	s_waitcnt lgkmcnt(0)
	v_pk_mul_f32 v[98:99], v[98:99], v[106:107]
	v_pk_fma_f32 v[110:111], v[114:115], v[110:111], v[100:101]
	v_pk_fma_f32 v[108:109], v[116:117], v[108:109], v[98:99]

.LBB0_159:
	v_lshlrev_b64 v[98:99], 12, v[198:199]
	v_lshl_add_u64 v[98:99], s[18:19], 0, v[98:99]
	v_mov_b32_e32 v131, v130
	s_waitcnt lgkmcnt(0)
	v_lshl_add_u64 v[106:107], v[186:187], 1, v[98:99]
	v_mov_b32_e32 v98, v130
	v_mov_b32_e32 v99, v130
	v_pk_mul_f32 v[100:101], v[92:93], v[98:99]
	v_pk_mul_f32 v[82:83], v[82:83], v[130:131]
	v_pk_mul_f32 v[104:105], v[90:91], v[130:131]
	v_pk_mul_f32 v[84:85], v[84:85], v[98:99]
	v_cvt_pk_bf16_f32 v90, v134, v135
	v_cvt_pk_bf16_f32 v91, v132, v133
	v_cvt_pk_bf16_f32 v92, v110, v111
	v_cvt_pk_bf16_f32 v93, v108, v109
	v_cvt_pk_bf16_f32 v98, v104, v105
	v_cvt_pk_bf16_f32 v99, v100, v101
	v_cvt_pk_bf16_f32 v100, v82, v83
	s_nop 0
	v_cvt_pk_bf16_f32 v101, v84, v85
	ds_read_b32 v82, v226 offset:576
	v_add_co_u32_e32 v84, vcc, s74, v106
	v_lshl_add_u64 v[102:103], v[106:107], 0, s[38:39]
	s_nop 0
	v_addc_co_u32_e32 v85, vcc, 0, v107, vcc
	s_waitcnt lgkmcnt(0)
	v_pk_mul_f32 v[80:81], v[80:81], v[82:83] op_sel_hi:[1,0]
	v_pk_mul_f32 v[78:79], v[78:79], v[82:83] op_sel_hi:[1,0]
	v_pk_mul_f32 v[76:77], v[76:77], v[82:83] op_sel_hi:[1,0]
	s_and_b64 vcc, exec, s[10:11]
	v_pk_mul_f32 v[74:75], v[74:75], v[82:83] op_sel_hi:[1,0]
	global_store_dwordx4 v[84:85], v[90:93], off
	global_store_dwordx4 v[102:103], v[98:101], off offset:64
	s_cbranch_vccnz .LBB0_163
	v_and_b32_e32 v84, 64, v225
	v_xor_b32_e32 v83, 16, v225
	v_add_u32_e32 v84, 64, v84
	v_cmp_lt_i32_e32 vcc, v83, v84
	s_nop 1
	v_cndmask_b32_e32 v83, v225, v83, vcc
	v_lshlrev_b32_e32 v83, 2, v83
	ds_bpermute_b32 v108, v83, v78
	ds_bpermute_b32 v90, v83, v74
	ds_bpermute_b32 v109, v83, v79
	ds_bpermute_b32 v91, v83, v75
	ds_bpermute_b32 v92, v83, v80
	ds_bpermute_b32 v84, v83, v76
	ds_bpermute_b32 v93, v83, v81
	ds_bpermute_b32 v85, v83, v77
	s_and_saveexec_b64 s[52:53], s[6:7]
	s_cbranch_execz .LBB0_162
	v_xor_b32_e32 v83, 0x80000000, v94
	v_xor_b32_e32 v98, 0x80000000, v95
	v_xor_b32_e32 v99, 0x80000000, v96
	v_xor_b32_e32 v100, 0x80000000, v97
	v_cndmask_b32_e64 v97, v97, v100, s[8:9]
	v_cndmask_b32_e64 v96, v96, v99, s[8:9]
	v_cndmask_b32_e64 v95, v95, v98, s[8:9]
	v_cndmask_b32_e64 v94, v94, v83, s[8:9]
	s_waitcnt lgkmcnt(5)
	v_pk_mul_f32 v[94:95], v[94:95], v[108:109]
	s_waitcnt lgkmcnt(1)
	v_pk_mul_f32 v[92:93], v[96:97], v[92:93]
	v_pk_fma_f32 v[78:79], v[230:231], v[78:79], v[94:95]
	v_pk_fma_f32 v[80:81], v[232:233], v[80:81], v[92:93]
	v_xor_b32_e32 v83, 0x80000000, v86
	v_xor_b32_e32 v92, 0x80000000, v87
	v_xor_b32_e32 v93, 0x80000000, v88
	v_xor_b32_e32 v94, 0x80000000, v89
	v_cndmask_b32_e64 v89, v89, v94, s[8:9]
	v_cndmask_b32_e64 v88, v88, v93, s[8:9]
	v_cndmask_b32_e64 v87, v87, v92, s[8:9]
	v_cndmask_b32_e64 v86, v86, v83, s[8:9]
	v_pk_mul_f32 v[86:87], v[86:87], v[90:91]
	s_waitcnt lgkmcnt(0)
	v_pk_mul_f32 v[84:85], v[88:89], v[84:85]
	v_pk_fma_f32 v[74:75], v[194:195], v[74:75], v[86:87]
	v_pk_fma_f32 v[76:77], v[196:197], v[76:77], v[84:85]

.LBB0_163:
	v_mov_b32_e32 v83, v82
	v_mov_b32_e32 v86, v82
	v_mov_b32_e32 v87, v82
	v_pk_mul_f32 v[50:51], v[50:51], v[82:83]
	v_pk_mul_f32 v[56:57], v[56:57], v[86:87]
	v_pk_mul_f32 v[88:89], v[54:55], v[82:83]
	v_pk_mul_f32 v[86:87], v[52:53], v[86:87]
	v_cvt_pk_bf16_f32 v52, v78, v79
	v_cvt_pk_bf16_f32 v53, v80, v81
	v_cvt_pk_bf16_f32 v54, v74, v75
	v_cvt_pk_bf16_f32 v55, v76, v77
	v_cvt_pk_bf16_f32 v74, v88, v89
	v_cvt_pk_bf16_f32 v75, v56, v57
	v_cvt_pk_bf16_f32 v76, v50, v51
	s_nop 0
	v_cvt_pk_bf16_f32 v77, v86, v87
	ds_read_b32 v50, v226 offset:640
	v_add_co_u32_e32 v56, vcc, s75, v106
	s_waitcnt lgkmcnt(1)
	v_lshl_add_u64 v[84:85], v[106:107], 0, s[40:41]
	v_addc_co_u32_e32 v57, vcc, 0, v107, vcc
	global_store_dwordx4 v[56:57], v[52:55], off
	global_store_dwordx4 v[84:85], v[74:77], off offset:64
	s_waitcnt lgkmcnt(0)
	v_pk_mul_f32 v[40:41], v[40:41], v[50:51] op_sel_hi:[1,0]
	v_pk_mul_f32 v[38:39], v[38:39], v[50:51] op_sel_hi:[1,0]
	v_pk_mul_f32 v[32:33], v[32:33], v[50:51] op_sel_hi:[1,0]
	s_and_b64 vcc, exec, s[10:11]
	v_pk_mul_f32 v[52:53], v[30:31], v[50:51] op_sel_hi:[1,0]
	s_cbranch_vccnz .LBB0_167
	v_and_b32_e32 v31, 64, v225
	v_xor_b32_e32 v30, 16, v225
	v_add_u32_e32 v31, 64, v31
	v_cmp_lt_i32_e32 vcc, v30, v31
	s_nop 1
	v_cndmask_b32_e32 v30, v225, v30, vcc
	v_lshlrev_b32_e32 v31, 2, v30
	ds_bpermute_b32 v74, v31, v38
	ds_bpermute_b32 v54, v31, v52
	ds_bpermute_b32 v75, v31, v39
	ds_bpermute_b32 v55, v31, v53
	ds_bpermute_b32 v56, v31, v40
	ds_bpermute_b32 v30, v31, v32
	ds_bpermute_b32 v57, v31, v41
	ds_bpermute_b32 v31, v31, v33
	s_and_saveexec_b64 s[52:53], s[6:7]
	s_cbranch_execz .LBB0_166
	v_xor_b32_e32 v51, 0x80000000, v70
	v_xor_b32_e32 v76, 0x80000000, v71
	v_xor_b32_e32 v77, 0x80000000, v72
	v_xor_b32_e32 v78, 0x80000000, v73
	v_cndmask_b32_e64 v73, v73, v78, s[8:9]
	v_cndmask_b32_e64 v72, v72, v77, s[8:9]
	v_cndmask_b32_e64 v71, v71, v76, s[8:9]
	v_cndmask_b32_e64 v70, v70, v51, s[8:9]
	s_waitcnt lgkmcnt(5)
	v_pk_mul_f32 v[70:71], v[70:71], v[74:75]
	s_waitcnt lgkmcnt(1)
	v_pk_mul_f32 v[56:57], v[72:73], v[56:57]
	v_pk_fma_f32 v[38:39], v[62:63], v[38:39], v[70:71]
	v_pk_fma_f32 v[40:41], v[64:65], v[40:41], v[56:57]
	v_xor_b32_e32 v51, 0x80000000, v66
	v_xor_b32_e32 v62, 0x80000000, v67
	v_xor_b32_e32 v56, 0x80000000, v68
	v_xor_b32_e32 v57, 0x80000000, v69
	v_cndmask_b32_e64 v57, v69, v57, s[8:9]
	v_cndmask_b32_e64 v56, v68, v56, s[8:9]
	v_cndmask_b32_e64 v63, v67, v62, s[8:9]
	v_cndmask_b32_e64 v62, v66, v51, s[8:9]
	v_pk_mul_f32 v[54:55], v[62:63], v[54:55]
	s_waitcnt lgkmcnt(0)
	v_pk_mul_f32 v[30:31], v[56:57], v[30:31]
	v_pk_fma_f32 v[52:53], v[58:59], v[52:53], v[54:55]
	v_pk_fma_f32 v[32:33], v[60:61], v[32:33], v[30:31]

.LBB0_167:
	v_mov_b32_e32 v51, v50
	s_waitcnt lgkmcnt(3)
	v_mov_b32_e32 v56, v50
	s_waitcnt lgkmcnt(1)
	v_mov_b32_e32 v57, v50
	v_pk_mul_f32 v[18:19], v[18:19], v[50:51]
	s_waitcnt lgkmcnt(0)
	v_lshlrev_b64 v[30:31], 12, v[198:199]
	v_pk_mul_f32 v[24:25], v[24:25], v[56:57]
	v_pk_mul_f32 v[58:59], v[22:23], v[50:51]
	v_pk_mul_f32 v[56:57], v[20:21], v[56:57]
	v_cvt_pk_bf16_f32 v20, v38, v39
	v_cvt_pk_bf16_f32 v21, v40, v41
	v_cvt_pk_bf16_f32 v22, v52, v53
	v_cvt_pk_bf16_f32 v23, v32, v33
	v_cvt_pk_bf16_f32 v38, v58, v59
	v_cvt_pk_bf16_f32 v39, v24, v25
	v_cvt_pk_bf16_f32 v40, v18, v19
	s_nop 0
	v_cvt_pk_bf16_f32 v41, v56, v57
	ds_read_b32 v18, v226 offset:704
	v_lshl_add_u64 v[30:31], s[18:19], 0, v[30:31]
	v_lshl_add_u64 v[30:31], v[186:187], 1, v[30:31]
	v_add_co_u32_e32 v24, vcc, s76, v30
	s_waitcnt lgkmcnt(0)
	v_pk_mul_f32 v[16:17], v[16:17], v[18:19] op_sel_hi:[1,0]
	v_addc_co_u32_e32 v25, vcc, 0, v31, vcc
	v_pk_mul_f32 v[14:15], v[14:15], v[18:19] op_sel_hi:[1,0]
	v_pk_mul_f32 v[12:13], v[12:13], v[18:19] op_sel_hi:[1,0]
	s_and_b64 vcc, exec, s[10:11]
	v_pk_mul_f32 v[10:11], v[10:11], v[18:19] op_sel_hi:[1,0]
	v_lshl_add_u64 v[54:55], v[30:31], 0, s[42:43]
	global_store_dwordx4 v[24:25], v[20:23], off
	global_store_dwordx4 v[54:55], v[38:41], off offset:64
	s_cbranch_vccnz .LBB0_171
	v_and_b32_e32 v20, 64, v225
	v_xor_b32_e32 v19, 16, v225
	v_add_u32_e32 v20, 64, v20
	v_cmp_lt_i32_e32 vcc, v19, v20
	s_nop 1
	v_cndmask_b32_e32 v19, v225, v19, vcc
	v_lshlrev_b32_e32 v19, 2, v19
	ds_bpermute_b32 v32, v19, v14
	ds_bpermute_b32 v22, v19, v10
	ds_bpermute_b32 v33, v19, v15
	ds_bpermute_b32 v23, v19, v11
	ds_bpermute_b32 v24, v19, v16
	ds_bpermute_b32 v20, v19, v12
	ds_bpermute_b32 v25, v19, v17
	ds_bpermute_b32 v21, v19, v13
	s_and_saveexec_b64 s[10:11], s[6:7]
	s_cbranch_execz .LBB0_170
	v_xor_b32_e32 v19, 0x80000000, v46
	v_xor_b32_e32 v40, 0x80000000, v47
	v_xor_b32_e32 v38, 0x80000000, v48
	v_xor_b32_e32 v39, 0x80000000, v49
	v_cndmask_b32_e64 v39, v49, v39, s[8:9]
	v_cndmask_b32_e64 v38, v48, v38, s[8:9]
	v_cndmask_b32_e64 v41, v47, v40, s[8:9]
	v_cndmask_b32_e64 v40, v46, v19, s[8:9]
	s_waitcnt lgkmcnt(5)
	v_pk_mul_f32 v[32:33], v[40:41], v[32:33]
	s_waitcnt lgkmcnt(1)
	v_pk_mul_f32 v[24:25], v[38:39], v[24:25]
	v_pk_fma_f32 v[14:15], v[42:43], v[14:15], v[32:33]
	v_pk_fma_f32 v[16:17], v[44:45], v[16:17], v[24:25]
	v_xor_b32_e32 v19, 0x80000000, v34
	v_xor_b32_e32 v32, 0x80000000, v35
	v_xor_b32_e32 v24, 0x80000000, v36
	v_xor_b32_e32 v25, 0x80000000, v37
	v_cndmask_b32_e64 v25, v37, v25, s[8:9]
	v_cndmask_b32_e64 v24, v36, v24, s[8:9]
	v_cndmask_b32_e64 v33, v35, v32, s[8:9]
	v_cndmask_b32_e64 v32, v34, v19, s[8:9]
	v_pk_mul_f32 v[22:23], v[32:33], v[22:23]
	s_waitcnt lgkmcnt(0)
	v_pk_mul_f32 v[20:21], v[24:25], v[20:21]
	v_pk_fma_f32 v[10:11], v[26:27], v[10:11], v[22:23]
	v_pk_fma_f32 v[12:13], v[28:29], v[12:13], v[20:21]

	.amdhsa_kernel _Z8mega_fwd5MArgs
		.amdhsa_group_segment_fixed_size 0
		.amdhsa_private_segment_fixed_size 0
		.amdhsa_kernarg_size 432
		.amdhsa_user_sgpr_count 2
		.amdhsa_user_sgpr_dispatch_ptr 0
		.amdhsa_user_sgpr_queue_ptr 0
		.amdhsa_user_sgpr_kernarg_segment_ptr 1
		.amdhsa_user_sgpr_dispatch_id 0
		.amdhsa_user_sgpr_kernarg_preload_length 0
		.amdhsa_user_sgpr_kernarg_preload_offset 0
		.amdhsa_user_sgpr_private_segment_size 0
		.amdhsa_uses_dynamic_stack 0
		.amdhsa_enable_private_segment 0
		.amdhsa_system_sgpr_workgroup_id_x 1
		.amdhsa_system_sgpr_workgroup_id_y 0
		.amdhsa_system_sgpr_workgroup_id_z 0
		.amdhsa_system_sgpr_workgroup_info 0
		.amdhsa_system_vgpr_workitem_id 0
		.amdhsa_next_free_vgpr 256
		.amdhsa_next_free_sgpr 102
		.amdhsa_accum_offset 256
		.amdhsa_reserve_vcc 1
		.amdhsa_float_round_mode_32 0
		.amdhsa_float_round_mode_16_64 0
		.amdhsa_float_denorm_mode_32 3
		.amdhsa_float_denorm_mode_16_64 3
		.amdhsa_dx10_clamp 1
		.amdhsa_ieee_mode 1
		.amdhsa_fp16_overflow 0
		.amdhsa_tg_split 0
		.amdhsa_exception_fp_ieee_invalid_op 0
		.amdhsa_exception_fp_denorm_src 0
		.amdhsa_exception_fp_ieee_div_zero 0
		.amdhsa_exception_fp_ieee_overflow 0
		.amdhsa_exception_fp_ieee_underflow 0
		.amdhsa_exception_fp_ieee_inexact 0
		.amdhsa_exception_int_div_zero 0
	.end_amdhsa_kernel

amdhsa.kernels:
  - .agpr_count:     0
    .args:
      - .offset:         0
        .size:           176
        .value_kind:     by_value
      - .offset:         176
        .size:           4
        .value_kind:     hidden_block_count_x
      - .offset:         180
        .size:           4
        .value_kind:     hidden_block_count_y
      - .offset:         184
        .size:           4
        .value_kind:     hidden_block_count_z
      - .offset:         188
        .size:           2
        .value_kind:     hidden_group_size_x
      - .offset:         190
        .size:           2
        .value_kind:     hidden_group_size_y
      - .offset:         192
        .size:           2
        .value_kind:     hidden_group_size_z
      - .offset:         194
        .size:           2
        .value_kind:     hidden_remainder_x
      - .offset:         196
        .size:           2
        .value_kind:     hidden_remainder_y
      - .offset:         198
        .size:           2
        .value_kind:     hidden_remainder_z
      - .offset:         216
        .size:           8
        .value_kind:     hidden_global_offset_x
      - .offset:         224
        .size:           8
        .value_kind:     hidden_global_offset_y
      - .offset:         232
        .size:           8
        .value_kind:     hidden_global_offset_z
      - .offset:         240
        .size:           2
        .value_kind:     hidden_grid_dims
      - .offset:         296
        .size:           4
        .value_kind:     hidden_dynamic_lds_size
    .group_segment_fixed_size: 0
    .kernarg_segment_align: 8
    .kernarg_segment_size: 432
    .language:       OpenCL C
    .language_version:
      - 2
      - 0
    .max_flat_workgroup_size: 512
    .name:           _Z8mega_fwd5MArgs
    .private_segment_fixed_size: 0
    .sgpr_count:     108
    .sgpr_spill_count: 41
    .symbol:         _Z8mega_fwd5MArgs.kd
    .uniform_work_group_size: 1
    .uses_dynamic_stack: false
    .vgpr_count:     256
    .vgpr_spill_count: 0
    .wavefront_size: 64
